# speedup vs baseline: 1.0063x; 1.0063x over previous
.Lrec_gate2:
	v_cndmask_b32_e64 v4, v2, v3, s[2:3]
	v_cndmask_b32_e64 v5, v6, v7, s[2:3]
	s_nop 0
	v_mov_b32_dpp v2, v4 row_ror:8 row_mask:0xf bank_mask:0xc
	v_mov_b32_dpp v3, v4 row_ror:8 row_mask:0xf bank_mask:0x3
	v_mov_b32_dpp v6, v5 row_ror:8 row_mask:0xf bank_mask:0xc
	v_mov_b32_dpp v7, v5 row_ror:8 row_mask:0xf bank_mask:0x3
	v_pk_fma_f32 v[2:3], v[2:3], s[40:41], v[112:113]
	v_pk_fma_f32 v[6:7], v[6:7], s[42:43], v[114:115]
	v_exp_f32_e32 v2, v2
	v_exp_f32_e32 v6, v6
	v_exp_f32_e32 v3, v3
	v_exp_f32_e32 v7, v7
	s_nop 0
	v_pk_add_f32 v[2:3], v[2:3], s[44:45]
	v_pk_add_f32 v[6:7], v[6:7], s[44:45]
	v_rcp_f32_e32 v6, v6
	v_rcp_f32_e32 v2, v2
	v_rcp_f32_e32 v3, v3
	v_rcp_f32_e32 v7, v7
	v_fma_f32 v0, v6, -2.0, 1.0
	v_mul_f32_e32 v0, v2, v0
	v_fmac_f32_e32 v0, v26, v3
	v_mul_f32_e32 v1, 0x4038aa3b, v0
	v_exp_f32_e32 v1, v1
	s_cmp_lg_u64 s[0:1], 0
	v_add_f32_e32 v1, 1.0, v1
	v_rcp_f32_e32 v1, v1
	s_nop 0
	v_fma_f32 v1, v1, -2.0, 1.0
	v_mul_f32_e32 v46, v7, v1
	v_cvt_f16_f32_e32 v2, v46
	v_bitop3_b16 v2, s37, v2, -2 bitop3:0xf8
	s_cbranch_scc1 .Lrec_pub_slow
	global_store_short v120, v2, s[8:9]
	s_branch .LBB2_29
